# final combine phases P13/P15: final_norm_w loaded once before the token loop instead of 4 dependent loads (+vmcnt(0) draining stores) per token
# speedup vs baseline: 1.0096x; 1.0095x over previous
; #define LAS __attribute__((address_space(3)))
; __device__ __forceinline__ float bflo(unsigned w) { return __uint_as_float(w << 16); }
; __device__ __forceinline__ float bfhi(unsigned w) { return __uint_as_float(w & 0xffff0000u); }
; __device__ __forceinline__ void p_final(const Args& a, const Frame& F, int half) {
;     moe_tables_load(a, F);
;     const int rowbase = half ? ((const LAS int*)(F.misc + LM_PSTART))[32] : 0;
;     const int X = 256 * ((const LAS int*)(F.misc + LM_CX))[0], tbeg = half ? X : 0, tend = half ? T : X;
;     const float* mod = (const float*)(a.ws + WS_MOD); const bf16* OUTK = (const bf16*)(a.ws + WS_OUTK);
;     const int* tok_row = (const int*)(a.ws + WS_TOK_ROW); const float* ent_w = (const float*)(a.ws + WS_ENT_W);
;     const int gw = F.bid * 8 + F.wave, NGW = F.G * 8;
;     const f32x4* fw = (const f32x4*)a.in[IN_FNW] + F.lane;
;     int rkn[4]; float wkn[4];
;     { const int t0 = tbeg + gw; if (t0 < tend) {
; #pragma unroll
;         for (int k = 0; k < 4; ++k) { rkn[k] = tok_row[t0 * 4 + k] - rowbase; wkn[k] = ent_w[t0 * 4 + k]; } } }
;     for (int t = tbeg + gw; t < tend; t += NGW) {
;         f32x4* xr = (f32x4*)(a.out + (size_t)t * D) + F.lane;
;         const u32x2* x1p = (const u32x2*)x1_row(a.out, a.ws, t) + F.lane;
;         const f32x4* g2 = (const f32x4*)(mod + (t >> 13) * 6144 + 5120) + F.lane;
;         int rk[4]; float wk[4];
; #pragma unroll
;         for (int k = 0; k < 4; ++k) { rk[k] = rkn[k]; wk[k] = wkn[k]; }
;         u32x2 ok[4][4], xw[4];
; #pragma unroll
;         for (int j = 0; j < 4; ++j) { xw[j] = x1p[64 * j];
; #pragma unroll
;             for (int k = 0; k < 4; ++k) ok[j][k] = *((const u32x2*)(OUTK + (size_t)rk[k] * D) + F.lane + 64 * j); }
;         { const int tn = t + NGW; if (tn < tend) {
; #pragma unroll
;             for (int k = 0; k < 4; ++k) { rkn[k] = tok_row[tn * 4 + k] - rowbase; wkn[k] = ent_w[tn * 4 + k]; } } }
;         f32x4 v[4]; float s = 0.f;
; #pragma unroll
;         for (int j = 0; j < 4; ++j) {
;             f32x4 m = (f32x4){0.f, 0.f, 0.f, 0.f};
; #pragma unroll
;             for (int k = 0; k < 4; ++k) { const u32x2 o = ok[j][k]; m.x += wk[k] * bflo(o.x); m.y += wk[k] * bfhi(o.x); m.z += wk[k] * bflo(o.y); m.w += wk[k] * bfhi(o.y); }
;             v[j] = (f32x4){bflo(xw[j].x), bfhi(xw[j].x), bflo(xw[j].y), bfhi(xw[j].y)} + g2[64 * j] * m;
.LBB0_1237:
	s_or_b64 exec, exec, s[6:7]
	s_add_i32 s4, 0, 0x22310
	v_mov_b32_e32 v1, s4
	s_waitcnt lgkmcnt(0)
	s_barrier
	ds_read_b32 v1, v1
	s_lshl_b32 s5, s2, 3
	s_waitcnt lgkmcnt(0)
	v_readfirstlane_b32 s4, v1
	s_lshl_b32 s14, s4, 8
	s_add_i32 s4, s96, s5
	s_cmp_ge_i32 s4, s14
	s_cbranch_scc1 .LBB0_1242
	s_add_u32 s15, s72, 0x900000
	s_addc_u32 s16, s73, 0
	s_add_u32 s17, s72, 0x400000
	s_addc_u32 s18, s73, 0
	s_lshl_b32 s8, s4, 2
	s_ashr_i32 s9, s8, 31
	s_lshl_b32 s6, s3, 3
	s_lshl_b64 s[8:9], s[8:9], 2
	s_add_u32 s10, s15, s8
	s_addc_u32 s11, s16, s9
	v_mov_b32_e32 v11, 0
	s_add_u32 s8, s17, s8
	s_addc_u32 s9, s18, s9
	global_load_dwordx4 v[2:5], v11, s[10:11]
	global_load_dwordx4 v[6:9], v11, s[8:9]
	v_mbcnt_lo_u32_b32 v1, -1, 0
	v_mbcnt_hi_u32_b32 v14, -1, v1
	v_and_b32_e32 v1, 64, v14
	v_add_u32_e32 v15, 64, v1
	v_xor_b32_e32 v1, 1, v14
	v_cmp_lt_i32_e32 vcc, v1, v15
	v_xor_b32_e32 v16, 2, v14
	s_add_u32 s19, s72, 0x3b200000
	v_cndmask_b32_e32 v1, v14, v1, vcc
	v_cmp_lt_i32_e32 vcc, v16, v15
	s_addc_u32 s20, s73, 0
	s_add_u32 s21, s70, 0x8000000
	v_cndmask_b32_e32 v16, v14, v16, vcc
	v_lshlrev_b32_e32 v62, 2, v16
	v_xor_b32_e32 v16, 4, v14
	v_cmp_lt_i32_e32 vcc, v16, v15
	s_addc_u32 s22, s71, 0
	s_add_i32 s7, s96, s6
	v_cndmask_b32_e32 v16, v14, v16, vcc
	v_lshlrev_b32_e32 v63, 2, v16
	v_xor_b32_e32 v16, 8, v14
	v_cmp_lt_i32_e32 vcc, v16, v15
	s_add_i32 s7, s7, s5
	s_mov_b64 s[8:9], 0x24900000
	v_cndmask_b32_e32 v16, v14, v16, vcc
	v_lshlrev_b32_e32 v64, 2, v16
	v_xor_b32_e32 v16, 16, v14
	v_cmp_lt_i32_e32 vcc, v16, v15
	s_lshl_b32 s5, s7, 2
	s_lshl_b32 s23, s3, 5
	v_cndmask_b32_e32 v16, v14, v16, vcc
	v_lshlrev_b32_e32 v65, 2, v16
	v_xor_b32_e32 v16, 32, v14
	v_cmp_lt_i32_e32 vcc, v16, v15
	v_mov_b32_e32 v15, v11
	s_ashr_i32 s7, s6, 31
	v_cndmask_b32_e32 v14, v14, v16, vcc
	v_lshlrev_b32_e32 v66, 2, v14
	v_lshlrev_b32_e32 v14, 3, v252
	v_lshl_add_u64 v[14:15], s[72:73], 0, v[14:15]
	v_lshl_add_u64 v[14:15], v[14:15], 0, s[8:9]
	s_or_b32 s8, s5, 3
	s_ashr_i32 s5, s4, 31
	s_lshl_b64 s[10:11], s[4:5], 12
	s_add_u32 s10, s70, s10
	v_lshlrev_b32_e32 v10, 4, v252
	s_addc_u32 s11, s71, s11
	v_lshl_add_u64 v[16:17], s[10:11], 0, v[10:11]
	s_mov_b64 s[10:11], 0xc00
	v_lshl_add_u64 v[12:13], s[68:69], 0, v[10:11]
	v_lshlrev_b32_e32 v1, 2, v1
	v_lshl_add_u64 v[16:17], v[16:17], 0, s[10:11]
	s_lshl_b64 s[10:11], s[6:7], 12
	v_lshlrev_b32_e32 v67, 3, v252
	s_mov_b64 s[12:13], 0x105000
	s_mov_b32 s24, 0x105000
	v_mov_b32_e32 v68, 0x358637bd
	s_mov_b32 s25, 0x800000
	global_load_dwordx4 v[120:123], v[12:13], off
	global_load_dwordx4 v[124:127], v[12:13], off offset:1024
	global_load_dwordx4 v[128:131], v[12:13], off offset:2048
	global_load_dwordx4 v[132:135], v[12:13], off offset:3072
	s_branch .LBB0_1240
.LBB0_1239:
	s_ashr_i32 s9, s4, 13
	s_mul_i32 s26, s9, 0x1800
	s_ashr_i32 s27, s26, 31
	s_lshl_b64 s[26:27], s[26:27], 2
	s_add_u32 s26, s72, s26
	s_addc_u32 s27, s73, s27
	v_lshlrev_b32_e32 v10, 4, v252
	v_lshl_add_u64 v[74:75], s[26:27], 0, v[10:11]
	v_add_co_u32_e32 v70, vcc, s24, v74
	v_lshl_add_u64 v[78:79], v[74:75], 0, s[12:13]
	s_nop 0
	v_addc_co_u32_e32 v71, vcc, 0, v75, vcc
	global_load_dwordx4 v[70:73], v[70:71], off
	s_waitcnt vmcnt(16)
	v_lshlrev_b32_e32 v80, 16, v54
	global_load_dwordx4 v[74:77], v[78:79], off offset:1024
	v_and_b32_e32 v81, 0xffff0000, v54
	v_lshlrev_b32_e32 v88, 16, v55
	v_and_b32_e32 v89, 0xffff0000, v55
	v_lshlrev_b32_e32 v90, 16, v52
	v_and_b32_e32 v91, 0xffff0000, v52
	v_lshlrev_b32_e32 v92, 16, v53
	v_and_b32_e32 v93, 0xffff0000, v53
	global_load_dwordx4 v[52:55], v[78:79], off offset:2048
	s_waitcnt vmcnt(17)
	v_lshlrev_b32_e32 v94, 16, v44
	v_and_b32_e32 v95, 0xffff0000, v44
	v_lshlrev_b32_e32 v44, 16, v45
	v_and_b32_e32 v45, 0xffff0000, v45
	v_lshlrev_b32_e32 v102, 16, v42
	v_and_b32_e32 v103, 0xffff0000, v42
	v_lshlrev_b32_e32 v104, 16, v43
	v_and_b32_e32 v105, 0xffff0000, v43
	s_waitcnt vmcnt(16)
	v_lshlrev_b32_e32 v42, 16, v34
	v_and_b32_e32 v43, 0xffff0000, v34
	v_pk_fma_f32 v[108:109], v[6:7], v[44:45], 0 op_sel_hi:[0,1,0]
	v_pk_fma_f32 v[110:111], v[6:7], v[42:43], 0 op_sel_hi:[0,1,0]
	global_load_dwordx4 v[42:45], v[78:79], off offset:3072
	s_waitcnt vmcnt(15)
	v_lshlrev_b32_e32 v82, 16, v56
	v_and_b32_e32 v83, 0xffff0000, v56
	v_lshlrev_b32_e32 v56, 16, v57
	v_and_b32_e32 v57, 0xffff0000, v57
	s_waitcnt vmcnt(14)
	v_lshlrev_b32_e32 v96, 16, v46
	v_and_b32_e32 v97, 0xffff0000, v46
	v_lshlrev_b32_e32 v46, 16, v47
	v_and_b32_e32 v47, 0xffff0000, v47
	v_pk_fma_f32 v[80:81], v[6:7], v[80:81], 0 op_sel_hi:[0,1,0]
	v_pk_fma_f32 v[88:89], v[6:7], v[88:89], 0 op_sel_hi:[0,1,0]
	v_pk_fma_f32 v[94:95], v[6:7], v[94:95], 0 op_sel_hi:[0,1,0]
	s_waitcnt vmcnt(11)
	v_lshlrev_b32_e32 v84, 16, v58
	v_and_b32_e32 v85, 0xffff0000, v58
	v_lshlrev_b32_e32 v58, 16, v59
	v_and_b32_e32 v59, 0xffff0000, v59
	s_waitcnt vmcnt(10)
	v_lshlrev_b32_e32 v98, 16, v48
	v_and_b32_e32 v99, 0xffff0000, v48
	v_lshlrev_b32_e32 v48, 16, v49
	v_and_b32_e32 v49, 0xffff0000, v49
	v_pk_fma_f32 v[80:81], v[6:7], v[82:83], v[80:81] op_sel:[1,0,0]
	v_pk_fma_f32 v[56:57], v[6:7], v[56:57], v[88:89] op_sel:[1,0,0]
	v_pk_fma_f32 v[78:79], v[6:7], v[96:97], v[94:95] op_sel:[1,0,0]
	v_pk_fma_f32 v[46:47], v[6:7], v[46:47], v[108:109] op_sel:[1,0,0]
	s_waitcnt vmcnt(7)
	v_lshlrev_b32_e32 v86, 16, v60
	v_and_b32_e32 v87, 0xffff0000, v60
	v_lshlrev_b32_e32 v60, 16, v61
	v_and_b32_e32 v61, 0xffff0000, v61
	s_waitcnt vmcnt(6)
; __device__ __forceinline__ float bflo(unsigned w) { return __uint_as_float(w << 16); }
; __device__ __forceinline__ float bfhi(unsigned w) { return __uint_as_float(w & 0xffff0000u); }
; __device__ __forceinline__ void p_final(const Args& a, const Frame& F, int half) {
;     ...
;         f32x4 v[4]; float s = 0.f;
; #pragma unroll
;         for (int j = 0; j < 4; ++j) {
;             f32x4 m = (f32x4){0.f, 0.f, 0.f, 0.f};
; #pragma unroll
;             for (int k = 0; k < 4; ++k) { const u32x2 o = ok[j][k]; m.x += wk[k] * bflo(o.x); m.y += wk[k] * bfhi(o.x); m.z += wk[k] * bflo(o.y); m.w += wk[k] * bfhi(o.y); }
;             v[j] = (f32x4){bflo(xw[j].x), bfhi(xw[j].x), bflo(xw[j].y), bfhi(xw[j].y)} + g2[64 * j] * m;
;             s += (v[j].x * v[j].x + v[j].y * v[j].y) + (v[j].z * v[j].z + v[j].w * v[j].w);
;         }
;         const float rstd = rsqrtf(wave_sum(s) * (1.f / D) + EPS);
; #pragma unroll
;         for (int j = 0; j < 4; ++j) xr[64 * j] = v[j] * rstd * fw[64 * j];
	v_lshlrev_b32_e32 v100, 16, v50
	v_and_b32_e32 v101, 0xffff0000, v50
	v_lshlrev_b32_e32 v50, 16, v51
	v_and_b32_e32 v51, 0xffff0000, v51
	v_pk_fma_f32 v[80:81], v[8:9], v[84:85], v[80:81] op_sel_hi:[0,1,1]
	v_pk_fma_f32 v[56:57], v[8:9], v[58:59], v[56:57] op_sel_hi:[0,1,1]
	v_pk_fma_f32 v[58:59], v[8:9], v[98:99], v[78:79] op_sel_hi:[0,1,1]
	v_pk_fma_f32 v[46:47], v[8:9], v[48:49], v[46:47] op_sel_hi:[0,1,1]
	v_pk_fma_f32 v[48:49], v[8:9], v[86:87], v[80:81] op_sel:[1,0,0]
	v_pk_fma_f32 v[56:57], v[8:9], v[60:61], v[56:57] op_sel:[1,0,0]
	v_pk_fma_f32 v[58:59], v[8:9], v[100:101], v[58:59] op_sel:[1,0,0]
	v_pk_fma_f32 v[46:47], v[8:9], v[50:51], v[46:47] op_sel:[1,0,0]
	v_lshlrev_b32_e32 v34, 16, v35
	v_and_b32_e32 v35, 0xffff0000, v35
	v_lshlrev_b32_e32 v106, 16, v36
	v_and_b32_e32 v107, 0xffff0000, v36
	v_pk_fma_f32 v[34:35], v[6:7], v[34:35], 0 op_sel_hi:[0,1,0]
	v_lshlrev_b32_e32 v36, 16, v37
	v_and_b32_e32 v37, 0xffff0000, v37
	v_pk_fma_f32 v[34:35], v[6:7], v[36:37], v[34:35] op_sel:[1,0,0]
	v_lshlrev_b32_e32 v36, 16, v39
	v_and_b32_e32 v37, 0xffff0000, v39
	v_pk_fma_f32 v[34:35], v[8:9], v[36:37], v[34:35] op_sel_hi:[0,1,1]
	s_waitcnt vmcnt(5)
	v_lshlrev_b32_e32 v36, 16, v41
	v_and_b32_e32 v37, 0xffff0000, v41
	v_pk_fma_f32 v[34:35], v[8:9], v[36:37], v[34:35] op_sel:[1,0,0]
	v_lshlrev_b32_e32 v36, 16, v32
	v_and_b32_e32 v37, 0xffff0000, v32
	v_lshlrev_b32_e32 v32, 16, v33
	s_waitcnt vmcnt(3)
	v_pk_fma_f32 v[50:51], v[56:57], v[72:73], v[92:93]
	v_pk_fma_f32 v[48:49], v[48:49], v[70:71], v[90:91]
	s_waitcnt vmcnt(2)
	v_pk_fma_f32 v[46:47], v[46:47], v[76:77], v[104:105]
	v_pk_fma_f32 v[56:57], v[58:59], v[74:75], v[102:103]
	v_pk_mul_f32 v[58:59], v[48:49], v[48:49]
	v_pk_mul_f32 v[60:61], v[50:51], v[50:51]
	v_pk_mul_f32 v[70:71], v[46:47], v[46:47]
	v_pk_mul_f32 v[72:73], v[56:57], v[56:57]
	v_pk_mov_b32 v[74:75], v[58:59], v[60:61] op_sel:[1,0]
	v_mov_b32_e32 v59, v61
	v_pk_mov_b32 v[60:61], v[72:73], v[70:71] op_sel:[1,0]
	v_mov_b32_e32 v73, v71
	v_pk_add_f32 v[60:61], v[60:61], v[72:73]
	v_pk_fma_f32 v[70:71], v[6:7], v[106:107], v[110:111] op_sel:[1,0,0]
	v_lshlrev_b32_e32 v72, 16, v38
	v_and_b32_e32 v73, 0xffff0000, v38
	v_pk_fma_f32 v[70:71], v[8:9], v[72:73], v[70:71] op_sel_hi:[0,1,1]
	v_lshlrev_b32_e32 v72, 16, v40
	v_and_b32_e32 v73, 0xffff0000, v40
	v_pk_fma_f32 v[70:71], v[8:9], v[72:73], v[70:71] op_sel:[1,0,0]
	v_and_b32_e32 v33, 0xffff0000, v33
	s_waitcnt vmcnt(1)
	v_pk_fma_f32 v[32:33], v[34:35], v[54:55], v[32:33]
	v_pk_fma_f32 v[34:35], v[70:71], v[52:53], v[36:37]
	v_lshlrev_b32_e32 v36, 16, v28
	v_and_b32_e32 v37, 0xffff0000, v28
	v_pk_fma_f32 v[36:37], v[6:7], v[36:37], 0 op_sel_hi:[0,1,0]
	v_lshlrev_b32_e32 v38, 16, v30
	v_and_b32_e32 v39, 0xffff0000, v30
	v_pk_fma_f32 v[36:37], v[6:7], v[38:39], v[36:37] op_sel:[1,0,0]
	v_lshlrev_b32_e32 v38, 16, v24
	v_and_b32_e32 v39, 0xffff0000, v24
	v_pk_fma_f32 v[36:37], v[8:9], v[38:39], v[36:37] op_sel_hi:[0,1,1]
	v_lshlrev_b32_e32 v38, 16, v26
	v_and_b32_e32 v39, 0xffff0000, v26
	v_lshlrev_b32_e32 v28, 16, v29
	v_and_b32_e32 v29, 0xffff0000, v29
	v_pk_fma_f32 v[36:37], v[8:9], v[38:39], v[36:37] op_sel:[1,0,0]
	v_pk_fma_f32 v[38:39], v[6:7], v[28:29], 0 op_sel_hi:[0,1,0]
	v_lshlrev_b32_e32 v40, 16, v31
	v_and_b32_e32 v41, 0xffff0000, v31
	v_pk_fma_f32 v[6:7], v[6:7], v[40:41], v[38:39] op_sel:[1,0,0]
	v_lshlrev_b32_e32 v24, 16, v25
	v_and_b32_e32 v25, 0xffff0000, v25
	v_pk_fma_f32 v[6:7], v[8:9], v[24:25], v[6:7] op_sel_hi:[0,1,1]
	v_lshlrev_b32_e32 v24, 16, v27
	v_and_b32_e32 v25, 0xffff0000, v27
	v_pk_fma_f32 v[6:7], v[8:9], v[24:25], v[6:7] op_sel:[1,0,0]
	v_lshlrev_b32_e32 v8, 16, v22
	v_and_b32_e32 v9, 0xffff0000, v22
	v_pk_add_f32 v[58:59], v[74:75], v[58:59]
	v_lshlrev_b32_e32 v22, 16, v23
	v_and_b32_e32 v23, 0xffff0000, v23
	s_waitcnt vmcnt(0)
	v_pk_fma_f32 v[36:37], v[36:37], v[42:43], v[8:9]
	v_pk_fma_f32 v[26:27], v[6:7], v[44:45], v[22:23]
	v_mul_f32_e32 v8, v36, v36
	v_pk_add_f32 v[6:7], v[58:59], v[58:59] op_sel:[0,1] op_sel_hi:[1,0]
	v_mul_f32_e32 v10, v37, v37
	v_mov_b32_e32 v7, v8
	v_pk_add_f32 v[8:9], v[60:61], v[60:61] op_sel:[0,1] op_sel_hi:[1,0]
	v_mul_f32_e32 v22, v26, v26
	v_mov_b32_e32 v9, v10
	v_pk_add_f32 v[6:7], v[6:7], v[8:9]
	v_mul_f32_e32 v8, v35, v35
	v_pk_fma_f32 v[8:9], v[34:35], v[34:35], v[8:9] op_sel_hi:[1,1,0]
	v_mul_f32_e32 v10, v33, v33
	v_mul_f32_e32 v24, v27, v27
	v_mov_b32_e32 v9, v22
	v_pk_fma_f32 v[22:23], v[32:33], v[32:33], v[10:11] op_sel_hi:[1,1,0]
	s_add_u32 s4, s4, s6
	v_mov_b32_e32 v23, v24
	v_pk_add_f32 v[8:9], v[8:9], v[22:23]
	s_addc_u32 s5, s5, s7
	v_pk_add_f32 v[6:7], v[6:7], v[8:9]
	s_add_i32 s8, s8, s23
	v_add_f32_e32 v6, v6, v7
	ds_bpermute_b32 v7, v1, v6
	s_cmp_lt_i32 s4, s14
	s_waitcnt lgkmcnt(0)
	v_add_f32_e32 v6, v6, v7
	ds_bpermute_b32 v7, v62, v6
	s_waitcnt lgkmcnt(0)
	v_add_f32_e32 v6, v6, v7
	ds_bpermute_b32 v7, v63, v6
	s_waitcnt lgkmcnt(0)
	v_add_f32_e32 v6, v6, v7
	ds_bpermute_b32 v7, v64, v6
	s_waitcnt lgkmcnt(0)
	v_add_f32_e32 v6, v6, v7
	ds_bpermute_b32 v7, v65, v6
	s_waitcnt lgkmcnt(0)
	v_add_f32_e32 v6, v6, v7
	ds_bpermute_b32 v7, v66, v6
	s_waitcnt lgkmcnt(0)
	v_add_f32_e32 v6, v6, v7
	v_fmamk_f32 v6, v6, 0x3a800000, v68
	v_mul_f32_e32 v7, 0x4b800000, v6
	v_cmp_gt_f32_e32 vcc, s25, v6
	s_nop 1
	v_cndmask_b32_e32 v6, v6, v7, vcc
	v_rsq_f32_e32 v6, v6
	s_nop 0
	v_mul_f32_e32 v7, 0x45800000, v6
	v_cndmask_b32_e32 v10, v6, v7, vcc
	v_pk_mul_f32 v[6:7], v[48:49], v[10:11] op_sel_hi:[1,0]
	v_pk_mul_f32 v[8:9], v[50:51], v[10:11] op_sel_hi:[1,0]
	s_waitcnt vmcnt(0)
	v_pk_mul_f32 v[6:7], v[120:121], v[6:7]
	v_pk_mul_f32 v[8:9], v[122:123], v[8:9]
	global_store_dwordx4 v[16:17], v[6:9], off offset:-3072
	v_pk_mul_f32 v[22:23], v[46:47], v[10:11] op_sel_hi:[1,0]
	v_pk_mul_f32 v[24:25], v[56:57], v[10:11] op_sel_hi:[1,0]
	v_pk_mul_f32 v[8:9], v[126:127], v[22:23]
	v_pk_mul_f32 v[6:7], v[124:125], v[24:25]
	global_store_dwordx4 v[16:17], v[6:9], off offset:-2048
	v_pk_mul_f32 v[22:23], v[32:33], v[10:11] op_sel_hi:[1,0]
	v_pk_mul_f32 v[24:25], v[34:35], v[10:11] op_sel_hi:[1,0]
	v_pk_mul_f32 v[8:9], v[130:131], v[22:23]
	v_pk_mul_f32 v[6:7], v[128:129], v[24:25]
	global_store_dwordx4 v[16:17], v[6:9], off offset:-1024
	s_nop 1
	v_mov_b64_e32 v[6:7], v[20:21]
	v_pk_mul_f32 v[8:9], v[26:27], v[10:11] op_sel_hi:[1,0]
	v_pk_mul_f32 v[20:21], v[36:37], v[10:11] op_sel_hi:[1,0]
	v_pk_mul_f32 v[20:21], v[132:133], v[20:21]
	v_pk_mul_f32 v[22:23], v[134:135], v[8:9]
	global_store_dwordx4 v[16:17], v[20:23], off
	v_lshl_add_u64 v[16:17], v[16:17], 0, s[10:11]
	v_mov_b64_e32 v[8:9], v[18:19]
	s_cbranch_scc0 .LBB0_1242
; __device__ __forceinline__ void p_final(const Args& a, const Frame& F, int half) {
;     ...
;         f32x4* xr = (f32x4*)(a.out + (size_t)t * D) + F.lane;
;         const u32x2* x1p = (const u32x2*)x1_row(a.out, a.ws, t) + F.lane;
;         const f32x4* g2 = (const f32x4*)(mod + (t >> 13) * 6144 + 5120) + F.lane;
;         int rk[4]; float wk[4];
; #pragma unroll
;         for (int k = 0; k < 4; ++k) { rk[k] = rkn[k]; wk[k] = wkn[k]; }
;         u32x2 ok[4][4], xw[4];
; #pragma unroll
;         for (int j = 0; j < 4; ++j) { xw[j] = x1p[64 * j];
; #pragma unroll
;             for (int k = 0; k < 4; ++k) ok[j][k] = *((const u32x2*)(OUTK + (size_t)rk[k] * D) + F.lane + 64 * j); }
;         { const int tn = t + NGW; if (tn < tend) {
; #pragma unroll
;             for (int k = 0; k < 4; ++k) { rkn[k] = tok_row[tn * 4 + k] - rowbase; wkn[k] = ent_w[tn * 4 + k]; } } }
.LBB0_1240:
	s_add_i32 s9, s4, 0xffff8800
	s_cmpk_lt_i32 s4, 0x7800
	s_cselect_b32 s27, s5, 0
	s_cselect_b32 s26, s4, s9
	s_waitcnt vmcnt(4)
	v_ashrrev_i32_e32 v23, 31, v4
	v_mov_b32_e32 v22, v4
	s_cselect_b32 s9, s22, s20
	s_cselect_b32 s28, s21, s19
	s_lshl_b64 s[26:27], s[26:27], 11
	v_lshlrev_b64 v[22:23], 11, v[22:23]
	s_add_u32 s26, s28, s26
	v_ashrrev_i32_e32 v19, 31, v2
	v_mov_b32_e32 v18, v2
	v_ashrrev_i32_e32 v21, 31, v3
	v_mov_b32_e32 v20, v3
	v_lshl_add_u64 v[70:71], v[14:15], 0, v[22:23]
	v_ashrrev_i32_e32 v23, 31, v5
	v_mov_b32_e32 v22, v5
	s_addc_u32 s27, s9, s27
	v_lshlrev_b64 v[18:19], 11, v[18:19]
	v_lshlrev_b64 v[20:21], 11, v[20:21]
	v_lshlrev_b64 v[22:23], 11, v[22:23]
	v_lshl_add_u64 v[18:19], v[14:15], 0, v[18:19]
	v_lshl_add_u64 v[20:21], v[14:15], 0, v[20:21]
	v_lshl_add_u64 v[72:73], v[14:15], 0, v[22:23]
	global_load_dwordx2 v[52:53], v67, s[26:27]
	global_load_dwordx2 v[42:43], v67, s[26:27] offset:512
	global_load_dwordx2 v[32:33], v67, s[26:27] offset:1024
	global_load_dwordx2 v[22:23], v67, s[26:27] offset:1536
	global_load_dwordx2 v[54:55], v[18:19], off
	global_load_dwordx2 v[44:45], v[18:19], off offset:512
	global_load_dwordx2 v[34:35], v[18:19], off offset:1024
	global_load_dwordx2 v[28:29], v[18:19], off offset:1536
	global_load_dwordx2 v[56:57], v[20:21], off
	global_load_dwordx2 v[46:47], v[20:21], off offset:512
	global_load_dwordx2 v[36:37], v[20:21], off offset:1024
	global_load_dwordx2 v[30:31], v[20:21], off offset:1536
	global_load_dwordx2 v[58:59], v[70:71], off
	global_load_dwordx2 v[48:49], v[70:71], off offset:512
	global_load_dwordx2 v[38:39], v[70:71], off offset:1024
	global_load_dwordx2 v[24:25], v[70:71], off offset:1536
	global_load_dwordx2 v[60:61], v[72:73], off
	global_load_dwordx2 v[50:51], v[72:73], off offset:512
	global_load_dwordx2 v[40:41], v[72:73], off offset:1024
	global_load_dwordx2 v[26:27], v[72:73], off offset:1536
	s_add_i32 s9, s6, s4
	s_cmp_ge_i32 s9, s14
	s_waitcnt vmcnt(24)
	v_mov_b64_e32 v[20:21], v[6:7]
	v_mov_b64_e32 v[18:19], v[8:9]
	s_cbranch_scc1 .LBB0_1239
	s_add_i32 s26, s8, -3
	s_ashr_i32 s27, s26, 31
	s_lshl_b64 s[26:27], s[26:27], 2
	s_add_u32 s28, s15, s26
	s_addc_u32 s29, s16, s27
	s_add_u32 s26, s17, s26
	s_addc_u32 s27, s18, s27
	s_add_i32 s34, s8, -2
	s_ashr_i32 s35, s34, 31
	s_lshl_b64 s[34:35], s[34:35], 2
	s_add_u32 s36, s15, s34
	s_addc_u32 s37, s16, s35
	s_add_u32 s34, s17, s34
	s_addc_u32 s35, s18, s35
	s_add_i32 s38, s8, -1
	s_ashr_i32 s39, s38, 31
	s_lshl_b64 s[38:39], s[38:39], 2
	s_add_u32 s40, s15, s38
	s_addc_u32 s41, s16, s39
	s_add_u32 s38, s17, s38
	s_addc_u32 s39, s18, s39
	s_ashr_i32 s9, s8, 31
	s_lshl_b64 s[42:43], s[8:9], 2
	s_add_u32 s44, s15, s42
	s_addc_u32 s45, s16, s43
	s_add_u32 s42, s17, s42
	s_addc_u32 s43, s18, s43
	global_load_dword v2, v11, s[28:29]
	global_load_dword v20, v11, s[26:27]
	global_load_dword v3, v11, s[36:37]
	global_load_dword v21, v11, s[34:35]
	global_load_dword v4, v11, s[40:41]
	global_load_dword v18, v11, s[38:39]
	global_load_dword v5, v11, s[44:45]
	global_load_dword v19, v11, s[42:43]
	s_branch .LBB0_1239

; #define LAS __attribute__((address_space(3)))
; __device__ __forceinline__ float bflo(unsigned w) { return __uint_as_float(w << 16); }
; __device__ __forceinline__ float bfhi(unsigned w) { return __uint_as_float(w & 0xffff0000u); }
; __device__ __forceinline__ void p_final(const Args& a, const Frame& F, int half) {
;     moe_tables_load(a, F);
;     const int rowbase = half ? ((const LAS int*)(F.misc + LM_PSTART))[32] : 0;
;     const int X = 256 * ((const LAS int*)(F.misc + LM_CX))[0], tbeg = half ? X : 0, tend = half ? T : X;
;     const float* mod = (const float*)(a.ws + WS_MOD); const bf16* OUTK = (const bf16*)(a.ws + WS_OUTK);
;     const int* tok_row = (const int*)(a.ws + WS_TOK_ROW); const float* ent_w = (const float*)(a.ws + WS_ENT_W);
;     const int gw = F.bid * 8 + F.wave, NGW = F.G * 8;
;     const f32x4* fw = (const f32x4*)a.in[IN_FNW] + F.lane;
;     int rkn[4]; float wkn[4];
;     { const int t0 = tbeg + gw; if (t0 < tend) {
; #pragma unroll
;         for (int k = 0; k < 4; ++k) { rkn[k] = tok_row[t0 * 4 + k] - rowbase; wkn[k] = ent_w[t0 * 4 + k]; } } }
;     for (int t = tbeg + gw; t < tend; t += NGW) {
;         f32x4* xr = (f32x4*)(a.out + (size_t)t * D) + F.lane;
;         const u32x2* x1p = (const u32x2*)x1_row(a.out, a.ws, t) + F.lane;
;         const f32x4* g2 = (const f32x4*)(mod + (t >> 13) * 6144 + 5120) + F.lane;
;         int rk[4]; float wk[4];
; #pragma unroll
;         for (int k = 0; k < 4; ++k) { rk[k] = rkn[k]; wk[k] = wkn[k]; }
;         u32x2 ok[4][4], xw[4];
; #pragma unroll
;         for (int j = 0; j < 4; ++j) { xw[j] = x1p[64 * j];
; #pragma unroll
;             for (int k = 0; k < 4; ++k) ok[j][k] = *((const u32x2*)(OUTK + (size_t)rk[k] * D) + F.lane + 64 * j); }
;         { const int tn = t + NGW; if (tn < tend) {
; #pragma unroll
;             for (int k = 0; k < 4; ++k) { rkn[k] = tok_row[tn * 4 + k] - rowbase; wkn[k] = ent_w[tn * 4 + k]; } } }
;         f32x4 v[4]; float s = 0.f;
; #pragma unroll
;         for (int j = 0; j < 4; ++j) {
;             f32x4 m = (f32x4){0.f, 0.f, 0.f, 0.f};
; #pragma unroll
;             for (int k = 0; k < 4; ++k) { const u32x2 o = ok[j][k]; m.x += wk[k] * bflo(o.x); m.y += wk[k] * bfhi(o.x); m.z += wk[k] * bflo(o.y); m.w += wk[k] * bfhi(o.y); }
;             v[j] = (f32x4){bflo(xw[j].x), bfhi(xw[j].x), bflo(xw[j].y), bfhi(xw[j].y)} + g2[64 * j] * m;
.LBB0_1393:
	s_or_b64 exec, exec, s[4:5]
	s_add_i32 s0, 0, 0x22310
	v_mov_b32_e32 v0, s0
	s_waitcnt lgkmcnt(0)
	s_barrier
	ds_read_b32 v0, v0
	s_lshl_b32 s6, s2, 3
	s_waitcnt lgkmcnt(0)
	v_readfirstlane_b32 s0, v0
	s_lshl_b32 s1, s0, 8
	s_add_i32 s0, s96, s6
	s_add_i32 s0, s0, s1
	s_cmp_gt_i32 s0, 0xffff
	s_cbranch_scc1 .LBB0_1398
	s_add_u32 s10, s72, 0x900000
	s_addc_u32 s11, s73, 0
	s_add_u32 s12, s72, 0x400000
	s_addc_u32 s13, s73, 0
	s_lshl_b32 s4, s0, 2
	s_ashr_i32 s5, s4, 31
	s_lshl_b32 s2, s3, 3
	s_add_i32 s7, 0, 0x22280
	s_lshl_b64 s[4:5], s[4:5], 2
	s_add_u32 s8, s10, s4
	s_addc_u32 s9, s11, s5
	v_mov_b32_e32 v5, 0
	s_add_u32 s4, s12, s4
	global_load_dwordx4 v[12:15], v5, s[8:9]
	s_addc_u32 s5, s13, s5
	global_load_dwordx4 v[0:3], v5, s[4:5]
	v_mbcnt_lo_u32_b32 v9, -1, 0
	v_mbcnt_hi_u32_b32 v10, -1, v9
	s_add_u32 s15, s72, 0x3b200000
	v_and_b32_e32 v11, 64, v10
	s_addc_u32 s16, s73, 0
	v_xor_b32_e32 v16, 1, v10
	v_add_u32_e32 v11, 64, v11
	s_add_u32 s17, s70, 0x8000000
	v_xor_b32_e32 v17, 2, v10
	v_mov_b32_e32 v22, s7
	v_cmp_lt_i32_e32 vcc, v16, v11
	s_addc_u32 s18, s71, 0
	s_add_i32 s7, s96, s1
	v_xor_b32_e32 v18, 4, v10
	v_cndmask_b32_e32 v16, v10, v16, vcc
	v_cmp_lt_i32_e32 vcc, v17, v11
	s_add_i32 s7, s7, s2
	v_lshlrev_b32_e32 v8, 3, v252
	v_mov_b32_e32 v9, v5
	v_xor_b32_e32 v19, 8, v10
	v_cndmask_b32_e32 v17, v10, v17, vcc
	v_cmp_lt_i32_e32 vcc, v18, v11
	s_add_i32 s7, s7, s6
	s_mov_b64 s[8:9], 0x24900000
	v_xor_b32_e32 v20, 16, v10
	v_lshl_add_u64 v[8:9], s[72:73], 0, v[8:9]
	v_cndmask_b32_e32 v18, v10, v18, vcc
	v_cmp_lt_i32_e32 vcc, v19, v11
	ds_read_b32 v61, v22
	s_ashr_i32 s1, s0, 31
	s_lshl_b32 s6, s7, 2
	v_xor_b32_e32 v21, 32, v10
	v_lshl_add_u64 v[8:9], v[8:9], 0, s[8:9]
	v_cndmask_b32_e32 v19, v10, v19, vcc
	v_cmp_lt_i32_e32 vcc, v20, v11
	s_lshl_b32 s19, s3, 5
	s_ashr_i32 s3, s2, 31
	s_lshl_b64 s[8:9], s[0:1], 12
	s_or_b32 s6, s6, 3
	v_cndmask_b32_e32 v20, v10, v20, vcc
	v_cmp_lt_i32_e32 vcc, v21, v11
	s_add_u32 s22, s70, s8
	v_lshlrev_b32_e32 v4, 4, v252
	v_cndmask_b32_e32 v10, v10, v21, vcc
	s_addc_u32 s23, s71, s9
	s_mov_b64 s[20:21], 0xc00
	v_lshlrev_b32_e32 v67, 2, v10
	v_lshl_add_u64 v[10:11], s[22:23], 0, v[4:5]
	v_lshlrev_b32_e32 v60, 3, v252
	s_mov_b64 s[4:5], 0x105000
	s_mov_b32 s14, 0x105000
	v_lshl_add_u64 v[6:7], s[68:69], 0, v[4:5]
	v_lshlrev_b32_e32 v62, 2, v16
	v_lshlrev_b32_e32 v63, 2, v17
	v_lshlrev_b32_e32 v64, 2, v18
	v_lshlrev_b32_e32 v65, 2, v19
	v_lshlrev_b32_e32 v66, 2, v20
	s_lshl_b64 s[8:9], s[2:3], 12
	v_lshl_add_u64 v[10:11], v[10:11], 0, s[20:21]
	v_mov_b32_e32 v68, 0x358637bd
	s_mov_b32 s20, 0x800000
	s_waitcnt vmcnt(1) lgkmcnt(0)
	v_sub_u32_e32 v13, v13, v61
	v_sub_u32_e32 v12, v12, v61
	v_sub_u32_e32 v15, v15, v61
	v_sub_u32_e32 v14, v14, v61
	global_load_dwordx4 v[120:123], v[6:7], off
	global_load_dwordx4 v[124:127], v[6:7], off offset:1024
	global_load_dwordx4 v[128:131], v[6:7], off offset:2048
	global_load_dwordx4 v[132:135], v[6:7], off offset:3072
	s_branch .LBB0_1396
.LBB0_1395:
	s_ashr_i32 s7, s0, 13
	s_mul_i32 s22, s7, 0x1800
	s_ashr_i32 s23, s22, 31
	s_lshl_b64 s[22:23], s[22:23], 2
	s_add_u32 s22, s72, s22
	s_addc_u32 s23, s73, s23
	v_lshlrev_b32_e32 v4, 4, v252
	v_lshl_add_u64 v[74:75], s[22:23], 0, v[4:5]
	v_add_co_u32_e32 v70, vcc, s14, v74
	v_lshl_add_u64 v[78:79], v[74:75], 0, s[4:5]
	s_nop 0
	v_addc_co_u32_e32 v71, vcc, 0, v75, vcc
	global_load_dwordx4 v[70:73], v[70:71], off
	s_waitcnt vmcnt(16)
	v_lshlrev_b32_e32 v80, 16, v52
	global_load_dwordx4 v[74:77], v[78:79], off offset:1024
	v_and_b32_e32 v81, 0xffff0000, v52
	v_lshlrev_b32_e32 v88, 16, v53
	v_and_b32_e32 v89, 0xffff0000, v53
	v_lshlrev_b32_e32 v90, 16, v50
	v_and_b32_e32 v91, 0xffff0000, v50
	v_lshlrev_b32_e32 v92, 16, v51
	v_and_b32_e32 v93, 0xffff0000, v51
	global_load_dwordx4 v[50:53], v[78:79], off offset:2048
	s_waitcnt vmcnt(17)
	v_lshlrev_b32_e32 v94, 16, v42
	v_and_b32_e32 v95, 0xffff0000, v42
	v_lshlrev_b32_e32 v42, 16, v43
	v_and_b32_e32 v43, 0xffff0000, v43
	v_lshlrev_b32_e32 v102, 16, v40
	v_and_b32_e32 v103, 0xffff0000, v40
	v_lshlrev_b32_e32 v104, 16, v41
	v_and_b32_e32 v105, 0xffff0000, v41
	s_waitcnt vmcnt(16)
	v_lshlrev_b32_e32 v40, 16, v32
	v_and_b32_e32 v41, 0xffff0000, v32
	v_pk_fma_f32 v[108:109], v[0:1], v[42:43], 0 op_sel_hi:[0,1,0]
	v_pk_fma_f32 v[110:111], v[0:1], v[40:41], 0 op_sel_hi:[0,1,0]
	global_load_dwordx4 v[40:43], v[78:79], off offset:3072
	s_waitcnt vmcnt(15)
	v_lshlrev_b32_e32 v82, 16, v54
	v_and_b32_e32 v83, 0xffff0000, v54
	v_lshlrev_b32_e32 v54, 16, v55
	v_and_b32_e32 v55, 0xffff0000, v55
	s_waitcnt vmcnt(14)
	v_lshlrev_b32_e32 v96, 16, v44
	v_and_b32_e32 v97, 0xffff0000, v44
	v_lshlrev_b32_e32 v44, 16, v45
	v_and_b32_e32 v45, 0xffff0000, v45
	v_pk_fma_f32 v[80:81], v[0:1], v[80:81], 0 op_sel_hi:[0,1,0]
	v_pk_fma_f32 v[88:89], v[0:1], v[88:89], 0 op_sel_hi:[0,1,0]
	v_pk_fma_f32 v[94:95], v[0:1], v[94:95], 0 op_sel_hi:[0,1,0]
	s_waitcnt vmcnt(11)
	v_lshlrev_b32_e32 v84, 16, v56
	v_and_b32_e32 v85, 0xffff0000, v56
	v_lshlrev_b32_e32 v56, 16, v57
	v_and_b32_e32 v57, 0xffff0000, v57
	s_waitcnt vmcnt(10)
	v_lshlrev_b32_e32 v98, 16, v46
	v_and_b32_e32 v99, 0xffff0000, v46
	v_lshlrev_b32_e32 v46, 16, v47
	v_and_b32_e32 v47, 0xffff0000, v47
	v_pk_fma_f32 v[80:81], v[0:1], v[82:83], v[80:81] op_sel:[1,0,0]
	v_pk_fma_f32 v[54:55], v[0:1], v[54:55], v[88:89] op_sel:[1,0,0]
	v_pk_fma_f32 v[78:79], v[0:1], v[96:97], v[94:95] op_sel:[1,0,0]
	v_pk_fma_f32 v[44:45], v[0:1], v[44:45], v[108:109] op_sel:[1,0,0]
	s_waitcnt vmcnt(7)
	v_lshlrev_b32_e32 v86, 16, v58
	v_and_b32_e32 v87, 0xffff0000, v58
	v_lshlrev_b32_e32 v58, 16, v59
	v_and_b32_e32 v59, 0xffff0000, v59
	s_waitcnt vmcnt(6)
; __device__ __forceinline__ float bflo(unsigned w) { return __uint_as_float(w << 16); }
; __device__ __forceinline__ float bfhi(unsigned w) { return __uint_as_float(w & 0xffff0000u); }
; __device__ __forceinline__ void p_final(const Args& a, const Frame& F, int half) {
;     ...
;         f32x4 v[4]; float s = 0.f;
; #pragma unroll
;         for (int j = 0; j < 4; ++j) {
;             f32x4 m = (f32x4){0.f, 0.f, 0.f, 0.f};
; #pragma unroll
;             for (int k = 0; k < 4; ++k) { const u32x2 o = ok[j][k]; m.x += wk[k] * bflo(o.x); m.y += wk[k] * bfhi(o.x); m.z += wk[k] * bflo(o.y); m.w += wk[k] * bfhi(o.y); }
;             v[j] = (f32x4){bflo(xw[j].x), bfhi(xw[j].x), bflo(xw[j].y), bfhi(xw[j].y)} + g2[64 * j] * m;
;             s += (v[j].x * v[j].x + v[j].y * v[j].y) + (v[j].z * v[j].z + v[j].w * v[j].w);
;         }
;         const float rstd = rsqrtf(wave_sum(s) * (1.f / D) + EPS);
; #pragma unroll
;         for (int j = 0; j < 4; ++j) xr[64 * j] = v[j] * rstd * fw[64 * j];
	v_lshlrev_b32_e32 v100, 16, v48
	v_and_b32_e32 v101, 0xffff0000, v48
	v_lshlrev_b32_e32 v48, 16, v49
	v_and_b32_e32 v49, 0xffff0000, v49
	v_pk_fma_f32 v[80:81], v[2:3], v[84:85], v[80:81] op_sel_hi:[0,1,1]
	v_pk_fma_f32 v[54:55], v[2:3], v[56:57], v[54:55] op_sel_hi:[0,1,1]
	v_pk_fma_f32 v[56:57], v[2:3], v[98:99], v[78:79] op_sel_hi:[0,1,1]
	v_pk_fma_f32 v[44:45], v[2:3], v[46:47], v[44:45] op_sel_hi:[0,1,1]
	v_pk_fma_f32 v[46:47], v[2:3], v[86:87], v[80:81] op_sel:[1,0,0]
	v_pk_fma_f32 v[54:55], v[2:3], v[58:59], v[54:55] op_sel:[1,0,0]
	v_pk_fma_f32 v[56:57], v[2:3], v[100:101], v[56:57] op_sel:[1,0,0]
	v_pk_fma_f32 v[44:45], v[2:3], v[48:49], v[44:45] op_sel:[1,0,0]
	v_lshlrev_b32_e32 v32, 16, v33
	v_and_b32_e32 v33, 0xffff0000, v33
	v_lshlrev_b32_e32 v106, 16, v34
	v_and_b32_e32 v107, 0xffff0000, v34
	v_pk_fma_f32 v[32:33], v[0:1], v[32:33], 0 op_sel_hi:[0,1,0]
	v_lshlrev_b32_e32 v34, 16, v35
	v_and_b32_e32 v35, 0xffff0000, v35
	v_pk_fma_f32 v[32:33], v[0:1], v[34:35], v[32:33] op_sel:[1,0,0]
	v_lshlrev_b32_e32 v34, 16, v37
	v_and_b32_e32 v35, 0xffff0000, v37
	v_pk_fma_f32 v[32:33], v[2:3], v[34:35], v[32:33] op_sel_hi:[0,1,1]
	s_waitcnt vmcnt(5)
	v_lshlrev_b32_e32 v34, 16, v39
	v_and_b32_e32 v35, 0xffff0000, v39
	v_pk_fma_f32 v[32:33], v[2:3], v[34:35], v[32:33] op_sel:[1,0,0]
	v_lshlrev_b32_e32 v34, 16, v30
	v_and_b32_e32 v35, 0xffff0000, v30
	v_lshlrev_b32_e32 v30, 16, v31
	s_waitcnt vmcnt(3)
	v_pk_fma_f32 v[48:49], v[54:55], v[72:73], v[92:93]
	v_pk_fma_f32 v[46:47], v[46:47], v[70:71], v[90:91]
	s_waitcnt vmcnt(2)
	v_pk_fma_f32 v[44:45], v[44:45], v[76:77], v[104:105]
	v_pk_fma_f32 v[54:55], v[56:57], v[74:75], v[102:103]
	v_pk_mul_f32 v[56:57], v[46:47], v[46:47]
	v_pk_mul_f32 v[58:59], v[48:49], v[48:49]
	v_pk_mul_f32 v[70:71], v[44:45], v[44:45]
	v_pk_mul_f32 v[72:73], v[54:55], v[54:55]
	v_pk_mov_b32 v[74:75], v[56:57], v[58:59] op_sel:[1,0]
	v_mov_b32_e32 v57, v59
	v_pk_mov_b32 v[58:59], v[72:73], v[70:71] op_sel:[1,0]
	v_mov_b32_e32 v73, v71
	v_pk_add_f32 v[58:59], v[58:59], v[72:73]
	v_pk_fma_f32 v[70:71], v[0:1], v[106:107], v[110:111] op_sel:[1,0,0]
	v_lshlrev_b32_e32 v72, 16, v36
	v_and_b32_e32 v73, 0xffff0000, v36
	v_pk_fma_f32 v[70:71], v[2:3], v[72:73], v[70:71] op_sel_hi:[0,1,1]
	v_lshlrev_b32_e32 v72, 16, v38
	v_and_b32_e32 v73, 0xffff0000, v38
	v_pk_fma_f32 v[70:71], v[2:3], v[72:73], v[70:71] op_sel:[1,0,0]
	v_and_b32_e32 v31, 0xffff0000, v31
	s_waitcnt vmcnt(1)
	v_pk_fma_f32 v[30:31], v[32:33], v[52:53], v[30:31]
	v_pk_fma_f32 v[32:33], v[70:71], v[50:51], v[34:35]
	v_lshlrev_b32_e32 v34, 16, v26
	v_and_b32_e32 v35, 0xffff0000, v26
	v_pk_fma_f32 v[34:35], v[0:1], v[34:35], 0 op_sel_hi:[0,1,0]
	v_lshlrev_b32_e32 v36, 16, v28
	v_and_b32_e32 v37, 0xffff0000, v28
	v_pk_fma_f32 v[34:35], v[0:1], v[36:37], v[34:35] op_sel:[1,0,0]
	v_lshlrev_b32_e32 v36, 16, v22
	v_and_b32_e32 v37, 0xffff0000, v22
	v_pk_fma_f32 v[34:35], v[2:3], v[36:37], v[34:35] op_sel_hi:[0,1,1]
	v_lshlrev_b32_e32 v36, 16, v24
	v_and_b32_e32 v37, 0xffff0000, v24
	v_lshlrev_b32_e32 v26, 16, v27
	v_and_b32_e32 v27, 0xffff0000, v27
	v_pk_fma_f32 v[34:35], v[2:3], v[36:37], v[34:35] op_sel:[1,0,0]
	v_pk_fma_f32 v[36:37], v[0:1], v[26:27], 0 op_sel_hi:[0,1,0]
	v_lshlrev_b32_e32 v38, 16, v29
	v_and_b32_e32 v39, 0xffff0000, v29
	v_pk_fma_f32 v[0:1], v[0:1], v[38:39], v[36:37] op_sel:[1,0,0]
	v_lshlrev_b32_e32 v22, 16, v23
	v_and_b32_e32 v23, 0xffff0000, v23
	v_pk_fma_f32 v[0:1], v[2:3], v[22:23], v[0:1] op_sel_hi:[0,1,1]
	v_lshlrev_b32_e32 v22, 16, v25
	v_and_b32_e32 v23, 0xffff0000, v25
	v_pk_fma_f32 v[0:1], v[2:3], v[22:23], v[0:1] op_sel:[1,0,0]
	v_lshlrev_b32_e32 v2, 16, v20
	v_and_b32_e32 v3, 0xffff0000, v20
	v_pk_add_f32 v[56:57], v[74:75], v[56:57]
	v_lshlrev_b32_e32 v20, 16, v21
	v_and_b32_e32 v21, 0xffff0000, v21
	s_waitcnt vmcnt(0)
	v_pk_fma_f32 v[34:35], v[34:35], v[40:41], v[2:3]
	v_pk_fma_f32 v[24:25], v[0:1], v[42:43], v[20:21]
	v_mul_f32_e32 v2, v34, v34
	v_pk_add_f32 v[0:1], v[56:57], v[56:57] op_sel:[0,1] op_sel_hi:[1,0]
	v_mul_f32_e32 v4, v35, v35
	v_mov_b32_e32 v1, v2
	v_pk_add_f32 v[2:3], v[58:59], v[58:59] op_sel:[0,1] op_sel_hi:[1,0]
	v_mul_f32_e32 v20, v24, v24
	v_mov_b32_e32 v3, v4
	v_pk_add_f32 v[0:1], v[0:1], v[2:3]
	v_mul_f32_e32 v2, v33, v33
	v_pk_fma_f32 v[2:3], v[32:33], v[32:33], v[2:3] op_sel_hi:[1,1,0]
	v_mul_f32_e32 v4, v31, v31
	v_mul_f32_e32 v22, v25, v25
	v_mov_b32_e32 v3, v20
	v_pk_fma_f32 v[20:21], v[30:31], v[30:31], v[4:5] op_sel_hi:[1,1,0]
	s_add_u32 s0, s0, s2
	v_mov_b32_e32 v21, v22
	v_pk_add_f32 v[2:3], v[2:3], v[20:21]
	s_addc_u32 s1, s1, s3
	v_pk_add_f32 v[0:1], v[0:1], v[2:3]
	s_add_i32 s6, s6, s19
	v_add_f32_e32 v0, v0, v1
	ds_bpermute_b32 v1, v62, v0
	s_cmp_lt_i32 s0, 0x10000
	s_waitcnt lgkmcnt(0)
	v_add_f32_e32 v0, v0, v1
	ds_bpermute_b32 v1, v63, v0
	s_waitcnt lgkmcnt(0)
	v_add_f32_e32 v0, v0, v1
	ds_bpermute_b32 v1, v64, v0
	s_waitcnt lgkmcnt(0)
	v_add_f32_e32 v0, v0, v1
	ds_bpermute_b32 v1, v65, v0
	s_waitcnt lgkmcnt(0)
	v_add_f32_e32 v0, v0, v1
	ds_bpermute_b32 v1, v66, v0
	s_waitcnt lgkmcnt(0)
	v_add_f32_e32 v0, v0, v1
	ds_bpermute_b32 v1, v67, v0
	s_waitcnt lgkmcnt(0)
	v_add_f32_e32 v0, v0, v1
	v_fmamk_f32 v0, v0, 0x3a800000, v68
	v_mul_f32_e32 v1, 0x4b800000, v0
	v_cmp_gt_f32_e32 vcc, s20, v0
	s_nop 1
	v_cndmask_b32_e32 v0, v0, v1, vcc
	v_rsq_f32_e32 v0, v0
	s_nop 0
	v_mul_f32_e32 v1, 0x45800000, v0
	v_cndmask_b32_e32 v4, v0, v1, vcc
	v_pk_mul_f32 v[0:1], v[46:47], v[4:5] op_sel_hi:[1,0]
	v_pk_mul_f32 v[2:3], v[48:49], v[4:5] op_sel_hi:[1,0]
	s_waitcnt vmcnt(0)
	v_pk_mul_f32 v[0:1], v[120:121], v[0:1]
	v_pk_mul_f32 v[2:3], v[122:123], v[2:3]
	global_store_dwordx4 v[10:11], v[0:3], off offset:-3072
	v_pk_mul_f32 v[20:21], v[44:45], v[4:5] op_sel_hi:[1,0]
	v_pk_mul_f32 v[22:23], v[54:55], v[4:5] op_sel_hi:[1,0]
	v_pk_mul_f32 v[2:3], v[126:127], v[20:21]
	v_pk_mul_f32 v[0:1], v[124:125], v[22:23]
	global_store_dwordx4 v[10:11], v[0:3], off offset:-2048
	v_pk_mul_f32 v[20:21], v[30:31], v[4:5] op_sel_hi:[1,0]
	v_pk_mul_f32 v[22:23], v[32:33], v[4:5] op_sel_hi:[1,0]
	v_pk_mul_f32 v[2:3], v[130:131], v[20:21]
	v_pk_mul_f32 v[0:1], v[128:129], v[22:23]
	global_store_dwordx4 v[10:11], v[0:3], off offset:-1024
	s_nop 1
	v_mov_b64_e32 v[0:1], v[18:19]
	v_pk_mul_f32 v[2:3], v[24:25], v[4:5] op_sel_hi:[1,0]
	v_pk_mul_f32 v[18:19], v[34:35], v[4:5] op_sel_hi:[1,0]
	v_pk_mul_f32 v[18:19], v[132:133], v[18:19]
	v_pk_mul_f32 v[20:21], v[134:135], v[2:3]
	global_store_dwordx4 v[10:11], v[18:21], off
	v_lshl_add_u64 v[10:11], v[10:11], 0, s[8:9]
	v_mov_b64_e32 v[2:3], v[16:17]
	s_cbranch_scc0 .LBB0_1398
; __device__ __forceinline__ void p_final(const Args& a, const Frame& F, int half) {
;     ...
;         f32x4* xr = (f32x4*)(a.out + (size_t)t * D) + F.lane;
;         const u32x2* x1p = (const u32x2*)x1_row(a.out, a.ws, t) + F.lane;
;         const f32x4* g2 = (const f32x4*)(mod + (t >> 13) * 6144 + 5120) + F.lane;
;         int rk[4]; float wk[4];
; #pragma unroll
;         for (int k = 0; k < 4; ++k) { rk[k] = rkn[k]; wk[k] = wkn[k]; }
;         u32x2 ok[4][4], xw[4];
; #pragma unroll
;         for (int j = 0; j < 4; ++j) { xw[j] = x1p[64 * j];
; #pragma unroll
;             for (int k = 0; k < 4; ++k) ok[j][k] = *((const u32x2*)(OUTK + (size_t)rk[k] * D) + F.lane + 64 * j); }
;         { const int tn = t + NGW; if (tn < tend) {
; #pragma unroll
;             for (int k = 0; k < 4; ++k) { rkn[k] = tok_row[tn * 4 + k] - rowbase; wkn[k] = ent_w[tn * 4 + k]; } } }
.LBB0_1396:
	s_add_i32 s7, s0, 0xffff8800
	s_cmpk_lt_i32 s0, 0x7800
	s_cselect_b32 s23, s1, 0
	s_cselect_b32 s22, s0, s7
	v_ashrrev_i32_e32 v21, 31, v14
	v_mov_b32_e32 v20, v14
	s_cselect_b32 s7, s18, s16
	s_cselect_b32 s21, s17, s15
	s_lshl_b64 s[22:23], s[22:23], 11
	v_lshlrev_b64 v[20:21], 11, v[20:21]
	s_add_u32 s22, s21, s22
	v_ashrrev_i32_e32 v17, 31, v12
	v_mov_b32_e32 v16, v12
	v_ashrrev_i32_e32 v19, 31, v13
	v_mov_b32_e32 v18, v13
	v_lshl_add_u64 v[70:71], v[8:9], 0, v[20:21]
	v_ashrrev_i32_e32 v21, 31, v15
	v_mov_b32_e32 v20, v15
	s_addc_u32 s23, s7, s23
	v_lshlrev_b64 v[16:17], 11, v[16:17]
	v_lshlrev_b64 v[18:19], 11, v[18:19]
	v_lshlrev_b64 v[20:21], 11, v[20:21]
	v_lshl_add_u64 v[16:17], v[8:9], 0, v[16:17]
	v_lshl_add_u64 v[18:19], v[8:9], 0, v[18:19]
	v_lshl_add_u64 v[72:73], v[8:9], 0, v[20:21]
	global_load_dwordx2 v[50:51], v60, s[22:23]
	global_load_dwordx2 v[40:41], v60, s[22:23] offset:512
	global_load_dwordx2 v[30:31], v60, s[22:23] offset:1024
	global_load_dwordx2 v[20:21], v60, s[22:23] offset:1536
	global_load_dwordx2 v[52:53], v[16:17], off
	global_load_dwordx2 v[42:43], v[16:17], off offset:512
	global_load_dwordx2 v[32:33], v[16:17], off offset:1024
	global_load_dwordx2 v[26:27], v[16:17], off offset:1536
	global_load_dwordx2 v[54:55], v[18:19], off
	global_load_dwordx2 v[44:45], v[18:19], off offset:512
	global_load_dwordx2 v[34:35], v[18:19], off offset:1024
	global_load_dwordx2 v[28:29], v[18:19], off offset:1536
	global_load_dwordx2 v[56:57], v[70:71], off
	global_load_dwordx2 v[46:47], v[70:71], off offset:512
	global_load_dwordx2 v[36:37], v[70:71], off offset:1024
	global_load_dwordx2 v[22:23], v[70:71], off offset:1536
	global_load_dwordx2 v[58:59], v[72:73], off
	global_load_dwordx2 v[48:49], v[72:73], off offset:512
	global_load_dwordx2 v[38:39], v[72:73], off offset:1024
	global_load_dwordx2 v[24:25], v[72:73], off offset:1536
	s_add_i32 s7, s2, s0
	s_cmp_gt_i32 s7, 0xffff
	s_waitcnt vmcnt(24)
	v_mov_b64_e32 v[18:19], v[0:1]
	v_mov_b64_e32 v[16:17], v[2:3]
	s_cbranch_scc1 .LBB0_1395
	s_add_i32 s22, s6, -3
	s_ashr_i32 s23, s22, 31
	s_lshl_b64 s[22:23], s[22:23], 2
	s_add_u32 s24, s10, s22
	s_addc_u32 s25, s11, s23
	s_add_u32 s22, s12, s22
	s_addc_u32 s23, s13, s23
	s_add_i32 s26, s6, -2
	s_ashr_i32 s27, s26, 31
	s_lshl_b64 s[26:27], s[26:27], 2
	s_add_u32 s28, s10, s26
	s_addc_u32 s29, s11, s27
	s_add_u32 s26, s12, s26
	s_addc_u32 s27, s13, s27
	s_add_i32 s30, s6, -1
	s_ashr_i32 s31, s30, 31
	s_lshl_b64 s[30:31], s[30:31], 2
	s_add_u32 s34, s10, s30
	s_addc_u32 s35, s11, s31
	s_add_u32 s30, s12, s30
	s_addc_u32 s31, s13, s31
	s_ashr_i32 s7, s6, 31
	s_lshl_b64 s[36:37], s[6:7], 2
	s_add_u32 s38, s10, s36
	s_addc_u32 s39, s11, s37
	s_add_u32 s36, s12, s36
	s_addc_u32 s37, s13, s37
	global_load_dword v4, v5, s[24:25]
	global_load_dword v18, v5, s[22:23]
	global_load_dword v12, v5, s[28:29]
	global_load_dword v19, v5, s[26:27]
	global_load_dword v14, v5, s[34:35]
	global_load_dword v16, v5, s[30:31]
	global_load_dword v15, v5, s[38:39]
	global_load_dword v17, v5, s[36:37]
	s_waitcnt vmcnt(5)
	v_sub_u32_e32 v13, v12, v61
	v_sub_u32_e32 v12, v4, v61
	s_waitcnt vmcnt(3)
	v_sub_u32_e32 v14, v14, v61
	s_waitcnt vmcnt(1)
	v_sub_u32_e32 v15, v15, v61
	s_branch .LBB0_1395
